# speedup vs baseline: 1.0195x; 1.0036x over previous
.LBB2_22:
	ds_read_b128 v[170:173], v174
	ds_read_b128 v[180:183], v174 offset:2048
	ds_read_b128 v[202:205], v178
	ds_read_b128 v[206:209], v178 offset:2048
	s_mov_b32 s89, s65
	s_mov_b32 s65, s6
	ds_read_b128 v[162:165], v194
	ds_read_b128 v[150:153], v194 offset:2048
	ds_read_b128 v[166:169], v195
	ds_read_b128 v[154:157], v195 offset:2048
	ds_read_b128 v[146:149], v194 offset:4096
	ds_read_b128 v[138:141], v194 offset:6144
	ds_read_b128 v[158:161], v195 offset:4096
	ds_read_b128 v[142:145], v195 offset:6144
	s_waitcnt vmcnt(14)
	s_mul_i32 s94, s83, s35
	v_cvt_pk_f16_f32 v22, v22, v23
	v_cvt_pk_f16_f32 v23, v24, v25
	v_cvt_pk_f16_f32 v18, v18, v19
	v_cvt_pk_f16_f32 v19, v20, v21
	v_cvt_pk_f16_f32 v14, v14, v15
	v_cvt_pk_f16_f32 v15, v16, v17
	v_cvt_pk_f16_f32 v10, v10, v11
	v_cvt_pk_f16_f32 v11, v12, v13
	ds_write2st64_b64 v201, v[22:23], v[18:19] offset0:32 offset1:40
	ds_write2st64_b64 v201, v[14:15], v[10:11] offset0:48 offset1:56
	s_nop 0
	s_lshl_b32 s6, s90, 6
	s_add_i32 s7, s94, s6
	s_lshl_b32 s7, s7, 2
	s_add_i32 s8, s7, s81
	s_add_i32 s9, s8, s81
	s_add_i32 s10, s9, s81
	buffer_load_dwordx4 v[22:25], v192, s[56:59], s7 offen nt
	buffer_load_dwordx4 v[18:21], v192, s[56:59], s8 offen nt
	buffer_load_dwordx4 v[14:17], v192, s[56:59], s9 offen nt
	buffer_load_dwordx4 v[10:13], v192, s[56:59], s10 offen nt
	s_waitcnt vmcnt(16)
	v_add_u32_e32 v210, s89, v193
	s_mul_i32 s95, s84, s35
	ds_write_b128 v210, v[6:9] offset:32768
	ds_write_b128 v210, v[2:5] offset:40960
	s_add_i32 s93, s95, s6
	s_nop 0
	s_barrier
	s_waitcnt lgkmcnt(0)
	s_setprio 1
	s_waitcnt lgkmcnt(11)
	v_mfma_f32_16x16x32_f16 v[134:137], v[170:173], v[162:165], v[134:137]
	v_mfma_f32_16x16x32_f16 v[130:133], v[180:183], v[162:165], v[130:133]
	s_waitcnt lgkmcnt(10)
	v_mfma_f32_16x16x32_f16 v[126:129], v[170:173], v[150:153], v[126:129]
	v_mfma_f32_16x16x32_f16 v[122:125], v[180:183], v[150:153], v[122:125]
	s_waitcnt lgkmcnt(7)
	v_mfma_f32_16x16x32_f16 v[118:121], v[170:173], v[146:149], v[118:121]
	v_mfma_f32_16x16x32_f16 v[114:117], v[180:183], v[146:149], v[114:117]
	s_waitcnt lgkmcnt(6)
	v_mfma_f32_16x16x32_f16 v[110:113], v[170:173], v[138:141], v[110:113]
	v_mfma_f32_16x16x32_f16 v[106:109], v[180:183], v[138:141], v[106:109]
	v_mfma_f32_16x16x32_f16 v[134:137], v[202:205], v[166:169], v[134:137]
	v_mfma_f32_16x16x32_f16 v[130:133], v[206:209], v[166:169], v[130:133]
	v_mfma_f32_16x16x32_f16 v[126:129], v[202:205], v[154:157], v[126:129]
	v_mfma_f32_16x16x32_f16 v[122:125], v[206:209], v[154:157], v[122:125]
	s_waitcnt lgkmcnt(5)
	v_mfma_f32_16x16x32_f16 v[118:121], v[202:205], v[158:161], v[118:121]
	v_mfma_f32_16x16x32_f16 v[114:117], v[206:209], v[158:161], v[114:117]
	s_waitcnt lgkmcnt(4)
	v_mfma_f32_16x16x32_f16 v[110:113], v[202:205], v[142:145], v[110:113]
	v_mfma_f32_16x16x32_f16 v[106:109], v[206:209], v[142:145], v[106:109]
	s_setprio 0
	s_barrier
	ds_read_b128 v[170:173], v174 offset:16384
	ds_read_b128 v[174:177], v174 offset:18432
	ds_read_b128 v[182:185], v178 offset:16384
	ds_read_b128 v[178:181], v178 offset:18432
	s_waitcnt vmcnt(14)
	s_cmp_lt_u32 s92, 32
	ds_write_b128 v210, v[30:33] offset:49152
	ds_write_b128 v210, v[26:29] offset:57344
	s_waitcnt vmcnt(13)
	s_cbranch_scc0 .LBB2_28
	s_add_i32 s38, s64, s92
	s_lshl_b64 s[60:61], s[38:39], 3
	s_add_u32 s60, s60, s85
	v_cmp_ne_u32_e64 s[6:7], 0, v34
	v_cmp_ne_u32_e64 s[8:9], 0, v35
	v_cmp_ne_u32_e64 s[10:11], 0, v36
	v_cmp_ne_u32_e64 s[12:13], 0, v37
	s_addc_u32 s61, s61, 0
	s_nop 1
	s_and_b64 s[98:99], s[6:7], s[8:9]
	s_and_b64 s[100:101], s[10:11], s[12:13]
	s_and_b64 s[98:99], s[98:99], s[100:101]
	s_cmp_eq_u64 s[98:99], -1
	s_cbranch_scc0 .Lqkv_mslow_0
	s_lshl_b64 s[96:97], s[60:61], 5
	v_lshl_add_u64 v[26:27], v[0:1], 0, s[96:97]
	v_mov_b32_e32 v28, -1
	v_mov_b32_e32 v29, -1
	s_add_u32 s6, s42, s60
	s_addc_u32 s7, s43, s61
	s_mov_b64 exec, 15
	global_store_dwordx2 v[26:27], v[28:29], off
	s_mov_b64 exec, 1
	global_store_byte v187, v187, s[6:7]
	s_mov_b64 exec, -1
	s_branch .LBB2_28

.LBB2_33:
	s_barrier
	s_waitcnt lgkmcnt(0)
	s_setprio 1
	s_waitcnt lgkmcnt(5)
	v_mfma_f32_16x16x32_f16 v[102:105], v[170:173], v[162:165], v[102:105]
	s_waitcnt lgkmcnt(4)
	v_mfma_f32_16x16x32_f16 v[98:101], v[174:177], v[162:165], v[98:101]
	v_mfma_f32_16x16x32_f16 v[94:97], v[170:173], v[150:153], v[94:97]
	v_mfma_f32_16x16x32_f16 v[90:93], v[174:177], v[150:153], v[90:93]
	v_mfma_f32_16x16x32_f16 v[86:89], v[170:173], v[146:149], v[86:89]
	v_mfma_f32_16x16x32_f16 v[82:85], v[174:177], v[146:149], v[82:85]
	v_mfma_f32_16x16x32_f16 v[78:81], v[170:173], v[138:141], v[78:81]
	v_mfma_f32_16x16x32_f16 v[74:77], v[174:177], v[138:141], v[74:77]
	s_waitcnt lgkmcnt(3)
	v_mfma_f32_16x16x32_f16 v[102:105], v[182:185], v[166:169], v[102:105]
	s_waitcnt lgkmcnt(2)
	v_mfma_f32_16x16x32_f16 v[98:101], v[178:181], v[166:169], v[98:101]
	v_mfma_f32_16x16x32_f16 v[94:97], v[182:185], v[154:157], v[94:97]
	v_mfma_f32_16x16x32_f16 v[90:93], v[178:181], v[154:157], v[90:93]
	v_mfma_f32_16x16x32_f16 v[86:89], v[182:185], v[158:161], v[86:89]
	v_mfma_f32_16x16x32_f16 v[82:85], v[178:181], v[158:161], v[82:85]
	v_mfma_f32_16x16x32_f16 v[78:81], v[182:185], v[142:145], v[78:81]
	v_mfma_f32_16x16x32_f16 v[74:77], v[178:181], v[142:145], v[74:77]
	s_setprio 0
	s_barrier
	v_add_u32_e32 v202, s89, v196
	v_add_u32_e32 v203, s89, v186
	ds_read_b128 v[170:173], v202 offset:32768
	ds_read_b128 v[174:177], v202 offset:34816
	ds_read_b128 v[178:181], v203 offset:32768
	ds_read_b128 v[182:185], v203 offset:34816
	ds_read_b128 v[162:165], v194 offset:16384
	ds_read_b128 v[150:153], v194 offset:18432
	ds_read_b128 v[166:169], v195 offset:16384
	ds_read_b128 v[154:157], v195 offset:18432
	ds_read_b128 v[146:149], v194 offset:20480
	ds_read_b128 v[138:141], v194 offset:22528
	ds_read_b128 v[158:161], v195 offset:20480
	ds_read_b128 v[142:145], v195 offset:22528
	s_waitcnt vmcnt(14)
	s_lshl_b32 s86, s90, 6
	v_cvt_pk_f16_f32 v58, v58, v59
	v_cvt_pk_f16_f32 v59, v60, v61
	v_cvt_pk_f16_f32 v54, v54, v55
	v_cvt_pk_f16_f32 v55, v56, v57
	v_cvt_pk_f16_f32 v50, v50, v51
	v_cvt_pk_f16_f32 v51, v52, v53
	v_cvt_pk_f16_f32 v46, v46, v47
	v_cvt_pk_f16_f32 v47, v48, v49
	ds_write2st64_b64 v201, v[58:59], v[54:55] offset1:8
	ds_write2st64_b64 v201, v[50:51], v[46:47] offset0:16 offset1:24
	s_nop 0
	s_add_i32 s6, s94, s86
	s_lshl_b32 s6, s6, 2
	s_add_i32 s7, s6, s81
	s_add_i32 s8, s7, s81
	s_add_i32 s9, s8, s81
	buffer_load_dwordx4 v[58:61], v192, s[56:59], s6 offen nt
	buffer_load_dwordx4 v[54:57], v192, s[56:59], s7 offen nt
	buffer_load_dwordx4 v[50:53], v192, s[56:59], s8 offen nt
	buffer_load_dwordx4 v[46:49], v192, s[56:59], s9 offen nt
	s_waitcnt vmcnt(16)
	v_add_u32_e32 v204, s87, v193
	ds_write_b128 v204, v[42:45] offset:32768
	ds_write_b128 v204, v[38:41] offset:40960
	s_nop 0
	s_barrier
	s_waitcnt lgkmcnt(0)
	s_setprio 1
	s_waitcnt lgkmcnt(11)
	v_mfma_f32_16x16x32_f16 v[134:137], v[170:173], v[162:165], v[134:137]
	v_mfma_f32_16x16x32_f16 v[130:133], v[174:177], v[162:165], v[130:133]
	s_waitcnt lgkmcnt(10)
	v_mfma_f32_16x16x32_f16 v[126:129], v[170:173], v[150:153], v[126:129]
	v_mfma_f32_16x16x32_f16 v[122:125], v[174:177], v[150:153], v[122:125]
	s_waitcnt lgkmcnt(7)
	v_mfma_f32_16x16x32_f16 v[118:121], v[170:173], v[146:149], v[118:121]
	v_mfma_f32_16x16x32_f16 v[114:117], v[174:177], v[146:149], v[114:117]
	s_waitcnt lgkmcnt(6)
	v_mfma_f32_16x16x32_f16 v[110:113], v[170:173], v[138:141], v[110:113]
	v_mfma_f32_16x16x32_f16 v[106:109], v[174:177], v[138:141], v[106:109]
	v_mfma_f32_16x16x32_f16 v[134:137], v[178:181], v[166:169], v[134:137]
	v_mfma_f32_16x16x32_f16 v[130:133], v[182:185], v[166:169], v[130:133]
	v_mfma_f32_16x16x32_f16 v[126:129], v[178:181], v[154:157], v[126:129]
	v_mfma_f32_16x16x32_f16 v[122:125], v[182:185], v[154:157], v[122:125]
	s_waitcnt lgkmcnt(5)
	v_mfma_f32_16x16x32_f16 v[118:121], v[178:181], v[158:161], v[118:121]
	v_mfma_f32_16x16x32_f16 v[114:117], v[182:185], v[158:161], v[114:117]
	s_waitcnt lgkmcnt(4)
	v_mfma_f32_16x16x32_f16 v[110:113], v[178:181], v[142:145], v[110:113]
	v_mfma_f32_16x16x32_f16 v[106:109], v[182:185], v[142:145], v[106:109]
	s_setprio 0
	s_barrier
	ds_read_b128 v[170:173], v202 offset:49152
	ds_read_b128 v[174:177], v202 offset:51200
	ds_read_b128 v[182:185], v203 offset:49152
	ds_read_b128 v[178:181], v203 offset:51200
	s_waitcnt vmcnt(14)
	s_cmp_gt_u32 s92, 30
	ds_write_b128 v204, v[66:69] offset:49152
	ds_write_b128 v204, v[62:65] offset:57344
	s_waitcnt vmcnt(13)
	s_cbranch_scc1 .LBB2_39
	s_add_i32 s38, s64, s92
	s_add_i32 s38, s38, 1
	s_lshl_b64 s[60:61], s[38:39], 3
	s_add_u32 s60, s60, s85
	v_cmp_ne_u32_e64 s[6:7], 0, v70
	v_cmp_ne_u32_e64 s[8:9], 0, v71
	v_cmp_ne_u32_e64 s[10:11], 0, v72
	v_cmp_ne_u32_e64 s[12:13], 0, v73
	s_addc_u32 s61, s61, 0
	s_nop 1
	s_and_b64 s[98:99], s[6:7], s[8:9]
	s_and_b64 s[100:101], s[10:11], s[12:13]
	s_and_b64 s[98:99], s[98:99], s[100:101]
	s_cmp_eq_u64 s[98:99], -1
	s_cbranch_scc0 .Lqkv_mslow_1
	s_lshl_b64 s[94:95], s[60:61], 5
	v_lshl_add_u64 v[62:63], v[0:1], 0, s[94:95]
	v_mov_b32_e32 v64, -1
	v_mov_b32_e32 v65, -1
	s_add_u32 s6, s42, s60
	s_addc_u32 s7, s43, s61
	s_mov_b64 exec, 15
	global_store_dwordx2 v[62:63], v[64:65], off
	s_mov_b64 exec, 1
	global_store_byte v187, v187, s[6:7]
	s_mov_b64 exec, -1
	s_branch .LBB2_39

.LBB2_48:
	s_endpgm
	s_nop 0
	s_nop 0
	s_nop 0
	s_nop 0
	s_nop 0
	s_nop 0
	s_nop 0
	s_nop 0
	s_nop 0
	s_nop 0
	s_nop 0
	s_endpgm
